# same rotation applied to the gate/up expert GEMM K-loop as well (8 loops)
# baseline (speedup 1.0000x reference)
.LBB0_2005:
	s_add_i32 s74, s74, 2
	s_and_b64 s[24:25], s[26:27], exec
	s_cselect_b32 s28, s66, s68
	s_cselect_b32 s29, s65, s69
	s_add_u32 s24, s28, 0x80
	s_addc_u32 s25, s29, 0
	s_waitcnt vmcnt(8)
	s_and_b64 s[26:27], s[26:27], exec
	s_waitcnt lgkmcnt(0)
	s_cselect_b32 s26, s20, s72
	s_cselect_b32 s27, s21, s73
	s_add_u32 s30, s26, 0x80
	s_addc_u32 s31, s27, 0
	s_barrier
	s_setprio 1
	s_waitcnt lgkmcnt(6)
	v_mfma_scale_f32_16x16x128_f8f6f4 v[194:197], v[18:25], v[58:65], v[194:197], v214, v214 op_sel_hi:[0,0,0]
	v_mfma_scale_f32_16x16x128_f8f6f4 v[186:189], v[26:33], v[58:65], v[186:189], v214, v214 op_sel_hi:[0,0,0]
	s_waitcnt lgkmcnt(4)
	v_mfma_scale_f32_16x16x128_f8f6f4 v[178:181], v[18:25], v[50:57], v[178:181], v214, v214 op_sel_hi:[0,0,0]
	v_mfma_scale_f32_16x16x128_f8f6f4 v[170:173], v[26:33], v[50:57], v[170:173], v214, v214 op_sel_hi:[0,0,0]
	s_waitcnt lgkmcnt(2)
	v_mfma_scale_f32_16x16x128_f8f6f4 v[162:165], v[18:25], v[42:49], v[162:165], v214, v214 op_sel_hi:[0,0,0]
	v_mfma_scale_f32_16x16x128_f8f6f4 v[154:157], v[26:33], v[42:49], v[154:157], v214, v214 op_sel_hi:[0,0,0]
	s_waitcnt lgkmcnt(0)
	v_mfma_scale_f32_16x16x128_f8f6f4 v[146:149], v[18:25], v[34:41], v[146:149], v214, v214 op_sel_hi:[0,0,0]
	v_mfma_scale_f32_16x16x128_f8f6f4 v[138:141], v[26:33], v[34:41], v[138:141], v214, v214 op_sel_hi:[0,0,0]
	s_setprio 0
	s_setprio 1
	v_mfma_scale_f32_16x16x128_f8f6f4 v[190:193], v[2:9], v[58:65], v[190:193], v214, v214 op_sel_hi:[0,0,0]
	v_mfma_scale_f32_16x16x128_f8f6f4 v[182:185], v[10:17], v[58:65], v[182:185], v214, v214 op_sel_hi:[0,0,0]
	v_mfma_scale_f32_16x16x128_f8f6f4 v[174:177], v[2:9], v[50:57], v[174:177], v214, v214 op_sel_hi:[0,0,0]
	v_mfma_scale_f32_16x16x128_f8f6f4 v[166:169], v[10:17], v[50:57], v[166:169], v214, v214 op_sel_hi:[0,0,0]
	v_mfma_scale_f32_16x16x128_f8f6f4 v[158:161], v[2:9], v[42:49], v[158:161], v214, v214 op_sel_hi:[0,0,0]
	v_mfma_scale_f32_16x16x128_f8f6f4 v[150:153], v[10:17], v[42:49], v[150:153], v214, v214 op_sel_hi:[0,0,0]
	v_mfma_scale_f32_16x16x128_f8f6f4 v[142:145], v[2:9], v[34:41], v[142:145], v214, v214 op_sel_hi:[0,0,0]
	v_mfma_scale_f32_16x16x128_f8f6f4 v[134:137], v[10:17], v[34:41], v[134:137], v214, v214 op_sel_hi:[0,0,0]
	s_setprio 0
	s_barrier
	ds_read_b128 v[34:37], v213 offset:16384
	ds_read_b128 v[38:41], v213 offset:17408
	ds_read_b128 v[42:45], v213 offset:18432
	ds_read_b128 v[46:49], v213 offset:19456
	ds_read_b128 v[50:53], v213 offset:20480
	ds_read_b128 v[54:57], v213 offset:21504
	ds_read_b128 v[58:61], v213 offset:22528
	ds_read_b128 v[62:65], v213 offset:23552
	s_mov_b32 s75, m0
	s_mov_b32 m0, s36
	s_nop 0
	global_load_lds_dwordx4 v207, s[26:27]
	s_mov_b32 m0, s75
	s_add_u32 s78, s26, 0x40000
	s_mov_b32 s75, m0
	s_mov_b32 m0, s37
	s_nop 0
	global_load_lds_dwordx4 v208, s[26:27]
	s_mov_b32 m0, s75
	s_addc_u32 s79, s27, 0
	s_mov_b32 s75, m0
	s_mov_b32 m0, s38
	s_nop 0
	global_load_lds_dwordx4 v207, s[78:79]
	s_mov_b32 m0, s75
	s_nop 0
	s_mov_b32 s75, m0
	s_mov_b32 m0, s39
	s_nop 0
	global_load_lds_dwordx4 v208, s[78:79]
	s_mov_b32 m0, s75
	s_nop 0
	s_mov_b32 s75, m0
	s_mov_b32 m0, s35
	s_nop 0
	global_load_lds_dwordx4 v66, s[28:29]
	s_mov_b32 m0, s75
	s_nop 0
	s_mov_b32 s75, m0
	s_mov_b32 m0, s40
	s_nop 0
	global_load_lds_dwordx4 v67, s[28:29]
	s_mov_b32 m0, s75
	s_waitcnt vmcnt(8)
	s_waitcnt lgkmcnt(0)
	s_barrier
	s_setprio 1
	s_waitcnt lgkmcnt(6)
	v_mfma_scale_f32_16x16x128_f8f6f4 v[130:133], v[18:25], v[34:41], v[130:133], v214, v214 op_sel_hi:[0,0,0]
	v_mfma_scale_f32_16x16x128_f8f6f4 v[122:125], v[26:33], v[34:41], v[122:125], v214, v214 op_sel_hi:[0,0,0]
	s_waitcnt lgkmcnt(4)
	v_mfma_scale_f32_16x16x128_f8f6f4 v[114:117], v[18:25], v[42:49], v[114:117], v214, v214 op_sel_hi:[0,0,0]
	v_mfma_scale_f32_16x16x128_f8f6f4 v[106:109], v[26:33], v[42:49], v[106:109], v214, v214 op_sel_hi:[0,0,0]
	s_waitcnt lgkmcnt(2)
	v_mfma_scale_f32_16x16x128_f8f6f4 v[98:101], v[18:25], v[50:57], v[98:101], v214, v214 op_sel_hi:[0,0,0]
	v_mfma_scale_f32_16x16x128_f8f6f4 v[90:93], v[26:33], v[50:57], v[90:93], v214, v214 op_sel_hi:[0,0,0]
	s_waitcnt lgkmcnt(0)
	v_mfma_scale_f32_16x16x128_f8f6f4 v[82:85], v[18:25], v[58:65], v[82:85], v214, v214 op_sel_hi:[0,0,0]
	v_mfma_scale_f32_16x16x128_f8f6f4 v[74:77], v[26:33], v[58:65], v[74:77], v214, v214 op_sel_hi:[0,0,0]
	s_setprio 0
	s_setprio 1
	v_mfma_scale_f32_16x16x128_f8f6f4 v[126:129], v[2:9], v[34:41], v[126:129], v214, v214 op_sel_hi:[0,0,0]
	v_mfma_scale_f32_16x16x128_f8f6f4 v[118:121], v[10:17], v[34:41], v[118:121], v214, v214 op_sel_hi:[0,0,0]
	v_mfma_scale_f32_16x16x128_f8f6f4 v[110:113], v[2:9], v[42:49], v[110:113], v214, v214 op_sel_hi:[0,0,0]
	v_mfma_scale_f32_16x16x128_f8f6f4 v[102:105], v[10:17], v[42:49], v[102:105], v214, v214 op_sel_hi:[0,0,0]
	v_mfma_scale_f32_16x16x128_f8f6f4 v[94:97], v[2:9], v[50:57], v[94:97], v214, v214 op_sel_hi:[0,0,0]
	v_mfma_scale_f32_16x16x128_f8f6f4 v[86:89], v[10:17], v[50:57], v[86:89], v214, v214 op_sel_hi:[0,0,0]
	v_mfma_scale_f32_16x16x128_f8f6f4 v[78:81], v[2:9], v[58:65], v[78:81], v214, v214 op_sel_hi:[0,0,0]
	v_mfma_scale_f32_16x16x128_f8f6f4 v[70:73], v[10:17], v[58:65], v[70:73], v214, v214 op_sel_hi:[0,0,0]
	s_setprio 0
	s_barrier
	v_add_u32_e32 v1, 0x18000, v210
	ds_read_b128 v[2:5], v1
	ds_read_b128 v[6:9], v1 offset:1024
	ds_read_b128 v[10:13], v1 offset:2048
	ds_read_b128 v[14:17], v1 offset:3072
	v_add_u32_e32 v1, 0x1c000, v210
	ds_read_b128 v[18:21], v1
	ds_read_b128 v[22:25], v1 offset:1024
	ds_read_b128 v[26:29], v1 offset:2048
	ds_read_b128 v[30:33], v1 offset:3072
	ds_read_b128 v[34:37], v213 offset:32768
	ds_read_b128 v[38:41], v213 offset:33792
	ds_read_b128 v[42:45], v213 offset:34816
	ds_read_b128 v[46:49], v213 offset:35840
	ds_read_b128 v[50:53], v213 offset:36864
	ds_read_b128 v[54:57], v213 offset:37888
	ds_read_b128 v[58:61], v213 offset:38912
	ds_read_b128 v[62:65], v213 offset:39936
	s_mov_b32 s75, m0
	s_mov_b32 m0, s41
	s_nop 0
	global_load_lds_dwordx4 v68, s[28:29]
	s_mov_b32 m0, s75
	s_nop 0
	s_mov_b32 s75, m0
	s_mov_b32 m0, s42
	s_nop 0
	global_load_lds_dwordx4 v69, s[28:29]
	s_mov_b32 m0, s75
	s_waitcnt vmcnt(8)
	s_waitcnt lgkmcnt(0)
	s_barrier
	s_setprio 1
	s_waitcnt lgkmcnt(6)
	v_mfma_scale_f32_16x16x128_f8f6f4 v[194:197], v[2:9], v[34:41], v[194:197], v214, v214 op_sel_hi:[0,0,0]
	v_mfma_scale_f32_16x16x128_f8f6f4 v[186:189], v[10:17], v[34:41], v[186:189], v214, v214 op_sel_hi:[0,0,0]
	s_waitcnt lgkmcnt(4)
	v_mfma_scale_f32_16x16x128_f8f6f4 v[178:181], v[2:9], v[42:49], v[178:181], v214, v214 op_sel_hi:[0,0,0]
	v_mfma_scale_f32_16x16x128_f8f6f4 v[170:173], v[10:17], v[42:49], v[170:173], v214, v214 op_sel_hi:[0,0,0]
	s_waitcnt lgkmcnt(2)
	v_mfma_scale_f32_16x16x128_f8f6f4 v[162:165], v[2:9], v[50:57], v[162:165], v214, v214 op_sel_hi:[0,0,0]
	v_mfma_scale_f32_16x16x128_f8f6f4 v[154:157], v[10:17], v[50:57], v[154:157], v214, v214 op_sel_hi:[0,0,0]
	s_waitcnt lgkmcnt(0)
	v_mfma_scale_f32_16x16x128_f8f6f4 v[146:149], v[2:9], v[58:65], v[146:149], v214, v214 op_sel_hi:[0,0,0]
	v_mfma_scale_f32_16x16x128_f8f6f4 v[138:141], v[10:17], v[58:65], v[138:141], v214, v214 op_sel_hi:[0,0,0]
	s_setprio 0
	s_setprio 1
	v_mfma_scale_f32_16x16x128_f8f6f4 v[190:193], v[18:25], v[34:41], v[190:193], v214, v214 op_sel_hi:[0,0,0]
	v_mfma_scale_f32_16x16x128_f8f6f4 v[182:185], v[26:33], v[34:41], v[182:185], v214, v214 op_sel_hi:[0,0,0]
	v_mfma_scale_f32_16x16x128_f8f6f4 v[174:177], v[18:25], v[42:49], v[174:177], v214, v214 op_sel_hi:[0,0,0]
	v_mfma_scale_f32_16x16x128_f8f6f4 v[166:169], v[26:33], v[42:49], v[166:169], v214, v214 op_sel_hi:[0,0,0]
	v_mfma_scale_f32_16x16x128_f8f6f4 v[158:161], v[18:25], v[50:57], v[158:161], v214, v214 op_sel_hi:[0,0,0]
	v_mfma_scale_f32_16x16x128_f8f6f4 v[150:153], v[26:33], v[50:57], v[150:153], v214, v214 op_sel_hi:[0,0,0]
	v_mfma_scale_f32_16x16x128_f8f6f4 v[142:145], v[18:25], v[58:65], v[142:145], v214, v214 op_sel_hi:[0,0,0]
	v_mfma_scale_f32_16x16x128_f8f6f4 v[134:137], v[26:33], v[58:65], v[134:137], v214, v214 op_sel_hi:[0,0,0]
	s_setprio 0
	s_barrier
	ds_read_b128 v[34:37], v213 offset:49152
	ds_read_b128 v[38:41], v213 offset:50176
	ds_read_b128 v[42:45], v213 offset:51200
	ds_read_b128 v[46:49], v213 offset:52224
	ds_read_b128 v[50:53], v213 offset:53248
	ds_read_b128 v[54:57], v213 offset:54272
	ds_read_b128 v[58:61], v213 offset:55296
	ds_read_b128 v[62:65], v213 offset:56320
	s_mov_b32 s28, m0
	s_mov_b32 m0, s44
	s_nop 0
	global_load_lds_dwordx4 v207, s[30:31]
	s_mov_b32 m0, s28
	s_add_u32 s26, s26, 0x40080
	s_mov_b32 s28, m0
	s_mov_b32 m0, s45
	s_nop 0
	global_load_lds_dwordx4 v208, s[30:31]
	s_mov_b32 m0, s28
	s_addc_u32 s27, s27, 0
	s_mov_b32 s28, m0
	s_mov_b32 m0, s52
	s_nop 0
	global_load_lds_dwordx4 v207, s[26:27]
	s_mov_b32 m0, s28
	s_nop 0
	s_mov_b32 s28, m0
	s_mov_b32 m0, s53
	s_nop 0
	global_load_lds_dwordx4 v208, s[26:27]
	s_mov_b32 m0, s28
	s_mov_b32 s26, m0
	s_mov_b32 m0, s46
	s_nop 0
	global_load_lds_dwordx4 v66, s[24:25]
	s_mov_b32 m0, s26
	s_nop 0
	s_mov_b32 s26, m0
	s_mov_b32 m0, s47
	s_nop 0
	global_load_lds_dwordx4 v67, s[24:25]
	s_mov_b32 m0, s26
	s_waitcnt vmcnt(8)
	s_waitcnt lgkmcnt(0)
	s_barrier
	s_setprio 1
	s_waitcnt lgkmcnt(6)
	v_mfma_scale_f32_16x16x128_f8f6f4 v[130:133], v[2:9], v[34:41], v[130:133], v214, v214 op_sel_hi:[0,0,0]
	v_mfma_scale_f32_16x16x128_f8f6f4 v[122:125], v[10:17], v[34:41], v[122:125], v214, v214 op_sel_hi:[0,0,0]
	s_waitcnt lgkmcnt(4)
	v_mfma_scale_f32_16x16x128_f8f6f4 v[114:117], v[2:9], v[42:49], v[114:117], v214, v214 op_sel_hi:[0,0,0]
	v_mfma_scale_f32_16x16x128_f8f6f4 v[106:109], v[10:17], v[42:49], v[106:109], v214, v214 op_sel_hi:[0,0,0]
	s_waitcnt lgkmcnt(2)
	v_mfma_scale_f32_16x16x128_f8f6f4 v[98:101], v[2:9], v[50:57], v[98:101], v214, v214 op_sel_hi:[0,0,0]
	v_mfma_scale_f32_16x16x128_f8f6f4 v[90:93], v[10:17], v[50:57], v[90:93], v214, v214 op_sel_hi:[0,0,0]
	s_waitcnt lgkmcnt(0)
	v_mfma_scale_f32_16x16x128_f8f6f4 v[82:85], v[2:9], v[58:65], v[82:85], v214, v214 op_sel_hi:[0,0,0]
	v_mfma_scale_f32_16x16x128_f8f6f4 v[74:77], v[10:17], v[58:65], v[74:77], v214, v214 op_sel_hi:[0,0,0]
	s_setprio 0
	s_setprio 1
	v_mfma_scale_f32_16x16x128_f8f6f4 v[126:129], v[18:25], v[34:41], v[126:129], v214, v214 op_sel_hi:[0,0,0]
	v_mfma_scale_f32_16x16x128_f8f6f4 v[118:121], v[26:33], v[34:41], v[118:121], v214, v214 op_sel_hi:[0,0,0]
	v_mfma_scale_f32_16x16x128_f8f6f4 v[110:113], v[18:25], v[42:49], v[110:113], v214, v214 op_sel_hi:[0,0,0]
	v_mfma_scale_f32_16x16x128_f8f6f4 v[102:105], v[26:33], v[42:49], v[102:105], v214, v214 op_sel_hi:[0,0,0]
	v_mfma_scale_f32_16x16x128_f8f6f4 v[94:97], v[18:25], v[50:57], v[94:97], v214, v214 op_sel_hi:[0,0,0]
	v_mfma_scale_f32_16x16x128_f8f6f4 v[86:89], v[26:33], v[50:57], v[86:89], v214, v214 op_sel_hi:[0,0,0]
	v_mfma_scale_f32_16x16x128_f8f6f4 v[78:81], v[18:25], v[58:65], v[78:81], v214, v214 op_sel_hi:[0,0,0]
	v_mfma_scale_f32_16x16x128_f8f6f4 v[70:73], v[26:33], v[58:65], v[70:73], v214, v214 op_sel_hi:[0,0,0]
	s_add_u32 s68, s68, 0x100
	s_addc_u32 s69, s69, 0
	s_add_u32 s72, s72, 0x100
	s_addc_u32 s73, s73, 0
	s_add_u32 s2, s2, 0x100
	s_addc_u32 s3, s3, 0
	s_cmp_ge_i32 s74, s15
	s_setprio 0
	s_barrier
	s_cbranch_scc1 .LBB0_2009
